# speedup vs baseline: 1.0032x; 1.0032x over previous
.Lattn_prio_done:
.LBB2_5:
	s_add_i32 s26, s26, 2
	v_add_u32_e32 v191, s3, v187
	ds_read_b64_tr_b16 v[176:177], v191 offset:24576
	ds_read_b64_tr_b16 v[178:179], v191 offset:25088
	v_mfma_f32_32x32x16_f16 v[96:111], v[172:175], v[124:127], v[32:47]
	v_exp_f32_e32 v56, v56
	v_exp_f32_e32 v57, v57
	v_cvt_pk_f16_f32 v140, v64, v65
	v_cvt_pk_f16_f32 v141, v66, v67
	ds_read_b64_tr_b16 v[172:173], v191 offset:28672
	ds_read_b64_tr_b16 v[174:175], v191 offset:29184
	v_mfma_f32_32x32x16_f16 v[80:95], v[168:171], v[124:127], v[32:47]
	v_exp_f32_e32 v58, v58
	v_exp_f32_e32 v59, v59
	v_pk_add_f16 v128, v140, v141
	v_cvt_pk_f16_f32 v142, v68, v69
	v_cvt_pk_f16_f32 v143, v70, v71
	ds_read_b64_tr_b16 v[64:65], v191 offset:25600
	ds_read_b64_tr_b16 v[66:67], v191 offset:26112
	v_mfma_f32_32x32x16_f16 v[96:111], v[164:167], v[120:123], v[96:111]
	v_exp_f32_e32 v60, v60
	v_exp_f32_e32 v61, v61
	v_pk_add_f16 v129, v142, v143
	v_cvt_pk_f16_f32 v136, v72, v73
	v_cvt_pk_f16_f32 v137, v74, v75
	ds_read_b64_tr_b16 v[68:69], v191 offset:29696
	ds_read_b64_tr_b16 v[70:71], v191 offset:30208
	v_mfma_f32_32x32x16_f16 v[80:95], v[160:163], v[120:123], v[80:95]
	v_exp_f32_e32 v62, v62
	v_exp_f32_e32 v63, v63
	v_pk_add_f16 v72, v136, v137
	v_pk_add_f16 v128, v128, v129
	v_cvt_pk_f16_f32 v138, v76, v77
	v_cvt_pk_f16_f32 v139, v78, v79
	s_min_u32 s2, s26, 28
	s_lshl_b32 s2, s2, 13
	s_add_u32 s2, s14, s2
	s_addc_u32 s3, s15, 0
	s_add_u32 s2, s2, 0x6000
	s_addc_u32 s3, s3, 0
	s_add_i32 s4, s31, s24
	s_mov_b32 s5, m0
	s_mov_b32 m0, s4
	s_nop 0
	global_load_lds_dwordx4 v189, s[2:3]
	s_mov_b32 m0, s5
	ds_read_b64_tr_b16 v[76:77], v191 offset:26624
	ds_read_b64_tr_b16 v[78:79], v191 offset:27136
	v_mfma_f32_32x32x16_f16 v[96:111], v[156:159], v[116:119], v[96:111]
	v_pk_add_f16 v73, v138, v139
	v_cvt_pk_f16_f32 v132, v48, v49
	v_cvt_pk_f16_f32 v133, v50, v51
	ds_read_b64_tr_b16 v[48:49], v191 offset:30720
	ds_read_b64_tr_b16 v[50:51], v191 offset:31232
	v_mfma_f32_32x32x16_f16 v[80:95], v[152:155], v[116:119], v[80:95]
	v_pk_add_f16 v129, v72, v73
	v_cvt_pk_f16_f32 v134, v52, v53
	v_cvt_pk_f16_f32 v135, v54, v55
	v_pk_add_f16 v156, v132, v133
	s_add_u32 s2, s27, 0x2000
	s_addc_u32 s3, s28, 0
	s_add_i32 s4, s29, s25
	s_mov_b32 s5, m0
	s_mov_b32 m0, s4
	s_nop 0
	global_load_lds_dwordx4 v189, s[2:3]
	s_mov_b32 m0, s5
	ds_read_b64_tr_b16 v[72:73], v191 offset:27648
	ds_read_b64_tr_b16 v[74:75], v191 offset:28160
	v_mfma_f32_32x32x16_f16 v[96:111], v[148:151], v[112:115], v[96:111]
	v_pk_add_f16 v153, v128, v129
	v_cvt_pk_f16_f32 v128, v56, v57
	v_cvt_pk_f16_f32 v129, v58, v59
	v_pk_add_f16 v152, v134, v135
	ds_read_b64_tr_b16 v[52:53], v191 offset:31744
	ds_read_b64_tr_b16 v[54:55], v191 offset:32256
	v_mfma_f32_32x32x16_f16 v[80:95], v[144:147], v[112:115], v[80:95]
	v_pk_add_f16 v56, v128, v129
	v_pk_add_f16 v57, v156, v152
	v_cvt_pk_f16_f32 v130, v60, v61
	v_cvt_pk_f16_f32 v131, v62, v63
	v_cndmask_b32_e64 v58, 0, 1, s[18:19]
	v_cmp_ne_u32_e64 s[2:3], 1, v58
	s_andn2_b64 vcc, exec, s[18:19]
	v_pk_add_f16 v57, v153, v57
	v_pk_add_f16 v58, v130, v131
	s_cbranch_vccnz .LBB2_7
	v_pk_add_f16 v59, v56, v58
	v_max3_f32 v61, v96, v97, v80
	v_max3_f32 v62, v98, v99, v81
	s_mov_b64 s[8:9], 0
	v_pk_add_f16 v59, v57, v59
	s_nop 0
	v_cvt_f32_f16_e32 v60, v59
	v_cvt_f32_f16_sdwa v59, v59 dst_sel:DWORD dst_unused:UNUSED_PAD src0_sel:WORD_1
	v_add_f32_e32 v59, v59, v60
	v_add_f32_e32 v188, v188, v59
	v_max3_f32 v59, v61, v82, v83
	v_max3_f32 v60, v62, v102, v103
	s_nop 0
	v_max3_f32 v59, v59, v100, v101
	v_max3_f32 v60, v60, v86, v87
	s_nop 0
	v_max3_f32 v59, v59, v84, v85
	v_max3_f32 v60, v60, v106, v107
	s_nop 0
	v_max3_f32 v59, v59, v104, v105
	v_max3_f32 v60, v60, v90, v91
	s_nop 0
	v_max3_f32 v59, v59, v88, v89
	v_max3_f32 v60, v60, v110, v111
	s_nop 0
	v_max3_f32 v59, v59, v108, v109
	v_max3_f32 v60, v60, v94, v95
	s_nop 0
	v_max3_f32 v59, v59, v92, v93
	s_nop 0
	v_max_f32 v59, v59, v60
	s_nop 0
	v_mov_b32_e32 v60, v59
	s_nop 1
	v_permlane32_swap_b32_e32 v59, v60
	v_max_f32 v59, v59, v60
	s_nop 0
	v_cmp_lt_f32_e32 vcc, s30, v59
	s_cbranch_vccnz .LBB2_19
.LBB2_7:
	s_waitcnt lgkmcnt(14)
	v_mfma_f32_32x32x16_f16 v[0:15], v[140:143], v[176:179], v[0:15]
	v_exp_f32_e32 v96, v96
	v_exp_f32_e32 v97, v97
	v_exp_f32_e32 v98, v98
	v_cndmask_b32_e64 v59, 0, 1, s[16:17]
	v_cmp_ne_u32_e64 s[4:5], 1, v59
	s_andn2_b64 vcc, exec, s[16:17]
	s_cbranch_vccnz .LBB2_9
	v_pk_add_f16 v56, v56, v58
	s_nop 0
	v_pk_add_f16 v56, v57, v56
	s_nop 0
	v_cvt_f32_f16_e32 v57, v56
	v_cvt_f32_f16_sdwa v56, v56 dst_sel:DWORD dst_unused:UNUSED_PAD src0_sel:WORD_1
	v_add_f32_e32 v56, v56, v57
	v_add_f32_e32 v188, v56, v188
